# speedup vs baseline: 1.0181x; 1.0000x over previous
_Z6k_gramILi0EEvPK15HIP_vector_typeIjLj4EEPyPf:
	s_load_dwordx4 s[8:11], s[0:1], 0x0
	s_load_dwordx2 s[4:5], s[0:1], 0x10
	s_lshl_b32 s0, s2, 2
	s_and_b32 s0, s0, 28
	s_ashr_i32 s1, s2, 6
	s_add_i32 s16, s0, s1
	v_readfirstlane_b32 s23, v0
	s_ashr_i32 s17, s16, 31
	s_lshr_b32 s21, s23, 6
	s_bfe_u32 s18, s23, 0x20006
	s_lshr_b32 s22, s2, 3
	s_bfe_u32 s20, s2, 0x30003
	s_lshl_b64 s[0:1], s[16:17], 20
	s_waitcnt lgkmcnt(0)
	s_add_u32 s12, s8, s0
	v_mov_b32_e32 v1, 0x20000
	s_addc_u32 s0, s9, s1
	s_lshl_b32 s1, s20, 2
	v_lshl_or_b32 v1, v0, 2, v1
	v_bfrev_b32_e32 v2, 1
	s_cmp_lt_u32 s20, 4
	ds_write_b32 v1, v2
	s_mov_b32 s24, 4
	s_mov_b32 s15, 0x20000
	s_and_b32 s13, s0, 0xffff
	s_mov_b32 s14, 0x100000
	v_lshlrev_b32_e32 v166, 4, v0
	s_lshl_b32 s25, s21, 10
	s_lshl_b32 s0, s20, 17
	s_mov_b32 m0, s25
	s_nop 0
	buffer_load_dwordx4 v166, s[12:15], s0 offen lds
	s_add_i32 s27, s25, 0x4000
	s_or_b32 s2, s0, 0x8000
	s_mov_b32 m0, s27
	s_nop 0
	buffer_load_dwordx4 v166, s[12:15], s2 offen lds
	s_add_i32 s34, s25, 0x10000
	s_or_b32 s2, s0, 0x10000
	s_mov_b32 m0, s34
	s_nop 0
	buffer_load_dwordx4 v166, s[12:15], s2 offen lds
	s_add_i32 s36, s25, 0x14000
	s_or_b32 s2, s0, 0x18000
	s_mov_b32 m0, s36
	s_nop 0
	buffer_load_dwordx4 v166, s[12:15], s2 offen lds
	s_add_i32 s26, s25, 0x2000
	s_or_b32 s2, s0, 0x2000
	s_mov_b32 m0, s26
	s_nop 0
	buffer_load_dwordx4 v166, s[12:15], s2 offen lds
	s_add_i32 s28, s25, 0x6000
	s_or_b32 s2, s0, 0xa000
	s_mov_b32 m0, s28
	s_nop 0
	buffer_load_dwordx4 v166, s[12:15], s2 offen lds
	s_add_i32 s35, s25, 0x12000
	s_or_b32 s2, s0, 0x12000
	s_mov_b32 m0, s35
	s_nop 0
	buffer_load_dwordx4 v166, s[12:15], s2 offen lds
	s_add_i32 s37, s25, 0x16000
	s_or_b32 s2, s0, 0x1a000
	s_mov_b32 m0, s37
	s_nop 0
	buffer_load_dwordx4 v166, s[12:15], s2 offen lds
	s_add_i32 s29, s25, 0x8000
	s_or_b32 s2, s0, 0x4000
	s_mov_b32 m0, s29
	s_nop 0
	buffer_load_dwordx4 v166, s[12:15], s2 offen lds
	s_add_i32 s31, s25, 0xc000
	s_or_b32 s2, s0, 0xc000
	s_mov_b32 m0, s31
	s_nop 0
	buffer_load_dwordx4 v166, s[12:15], s2 offen lds
	s_add_i32 s38, s25, 0x18000
	s_or_b32 s2, s0, 0x14000
	s_mov_b32 m0, s38
	s_nop 0
	buffer_load_dwordx4 v166, s[12:15], s2 offen lds
	s_add_i32 s40, s25, 0x1c000
	s_or_b32 s2, s0, 0x1c000
	s_mov_b32 m0, s40
	s_nop 0
	buffer_load_dwordx4 v166, s[12:15], s2 offen lds
	s_add_i32 s30, s25, 0xa000
	s_or_b32 s2, s0, 0x6000
	s_mov_b32 m0, s30
	s_nop 0
	buffer_load_dwordx4 v166, s[12:15], s2 offen lds
	s_add_i32 s33, s25, 0xe000
	s_or_b32 s2, s0, 0xe000
	s_mov_b32 m0, s33
	s_nop 0
	buffer_load_dwordx4 v166, s[12:15], s2 offen lds
	s_add_i32 s39, s25, 0x1a000
	s_or_b32 s2, s0, 0x16000
	s_mov_b32 m0, s39
	s_nop 0
	buffer_load_dwordx4 v166, s[12:15], s2 offen lds
	s_add_i32 s42, s25, 0x1e000
	s_or_b32 s2, s0, 0x1e000
	s_mov_b32 m0, s42
	s_nop 0
	buffer_load_dwordx4 v166, s[12:15], s2 offen lds
	s_lshl_b32 s0, s23, 9
	s_lshl_b32 s2, s23, 8
	v_and_b32_e32 v167, 15, v0
	v_bfe_u32 v160, v0, 4, 2
	s_and_b32 s0, s0, 0x10000
	s_and_b32 s2, s2, 0x4000
	v_lshlrev_b32_e32 v128, 9, v160
	v_lshlrev_b32_e32 v129, 4, v167
	s_or_b32 s0, s0, s2
	v_or3_b32 v124, s0, v128, v129
	s_waitcnt vmcnt(12)
	s_waitcnt lgkmcnt(0)
	s_barrier
	s_lshr_b32 s41, s23, 8
	s_lshl_b32 s0, s41, 14
	s_lshl_b32 s50, s24, 2
	v_or3_b32 v168, s0, v128, v129
	s_or_b32 s43, s18, s1
	s_lshl_b32 s0, s16, 10
	s_lshl_b32 s1, s43, 5
	ds_read_b128 v[128:131], v168
	ds_read_b128 v[132:135], v168 offset:256
	ds_read_b128 v[136:139], v168 offset:2048
	ds_read_b128 v[140:143], v168 offset:2304
	s_or_b32 s0, s1, s0
	v_or_b32_e32 v144, s0, v167
	v_lshlrev_b32_e32 v146, 2, v160
	v_ashrrev_i32_e32 v145, 31, v144
	v_lshl_add_u64 v[164:165], v[144:145], 2, s[4:5]
	v_or_b32_e32 v144, 1, v146
	v_cmp_eq_u32_e64 s[2:3], v144, v167
	v_or_b32_e32 v144, 2, v146
	v_cmp_eq_u32_e64 s[4:5], v144, v167
	v_or_b32_e32 v144, 3, v146
	s_add_i32 s44, s50, 3
	s_lshl_b32 s45, s22, 2
	v_cmp_eq_u32_e64 s[0:1], v146, v167
	v_cmp_eq_u32_e64 s[6:7], v144, v167
	v_add_u32_e32 v169, 0x10000, v168
	v_add_u32_e32 v170, 0x10100, v168
	v_add_u32_e32 v171, 0x10800, v168
	v_add_u32_e32 v172, 0x10900, v168
	s_and_b32 s8, s45, 28
	s_add_i32 s8, s8, s41
	s_lshl_b32 s19, s8, 1
	s_or_b32 s51, s19, 1
	v_mov_b32_e32 v234, s19
	v_mov_b32_e32 v235, s51
	s_and_b32 s46, s21, 3
	s_lshl_b32 s46, s46, 5
	v_lshl_or_b32 v173, v160, 3, s46
	s_lshl_b32 s47, s41, 7
	s_mov_b32 s48, 0
	s_movk_i32 s49, 0xffc0
	v_add_u32_e32 v174, 0x11000, v168
	v_add_u32_e32 v175, 0x11100, v168
	v_add_u32_e32 v176, 0x11800, v168
	v_add_u32_e32 v177, 0x11900, v168
	v_add_u32_e32 v178, 0x12000, v168
	v_add_u32_e32 v179, 0x12100, v168
	v_add_u32_e32 v180, 0x12800, v168
	v_add_u32_e32 v181, 0x12900, v168
	v_add_u32_e32 v182, 0x13000, v168
	v_add_u32_e32 v183, 0x13100, v168
	v_add_u32_e32 v184, 0x13800, v168
	v_add_u32_e32 v185, 0x13900, v168
	v_add_u32_e32 v186, 0x18000, v168
	v_add_u32_e32 v187, 0x18100, v168
	v_add_u32_e32 v188, 0x18800, v168
	v_add_u32_e32 v189, 0x18900, v168
	v_add_u32_e32 v190, 0x19000, v168
	v_add_u32_e32 v191, 0x19100, v168
	v_add_u32_e32 v192, 0x19800, v168
	v_add_u32_e32 v193, 0x19900, v168
	v_add_u32_e32 v194, 0x1a000, v168
	v_add_u32_e32 v195, 0x1a100, v168
	v_add_u32_e32 v196, 0x1a800, v168
	v_add_u32_e32 v197, 0x1a900, v168
	v_add_u32_e32 v198, 0x1b000, v168
	v_add_u32_e32 v199, 0x1b100, v168
	v_add_u32_e32 v200, 0x1b800, v168
	v_add_u32_e32 v201, 0x1b900, v168
	ds_read_b128 v[0:3], v124
	ds_read_b128 v[4:7], v124 offset:256
	ds_read_b128 v[8:11], v124 offset:2048
	ds_read_b128 v[12:15], v124 offset:2304
	ds_read_b128 v[144:147], v168
	ds_read_b128 v[148:151], v168 offset:256
	ds_read_b128 v[152:155], v168 offset:2048
	ds_read_b128 v[156:159], v168 offset:2304
	ds_read_b128 v[224:227], v168 offset:4096
	s_waitcnt lgkmcnt(4)
	v_mfma_f32_16x16x32_bf16 v[208:211], v[0:3], v[144:147], 0
	v_mfma_f32_16x16x32_bf16 v[212:215], v[4:7], v[144:147], 0
	ds_read_b128 v[228:231], v168 offset:4352
	ds_read_b128 v[16:19], v124 offset:4096
	ds_read_b128 v[20:23], v124 offset:4352
	s_waitcnt lgkmcnt(6)
	v_mfma_f32_16x16x32_bf16 v[216:219], v[0:3], v[148:151], 0
	v_mfma_f32_16x16x32_bf16 v[220:223], v[4:7], v[148:151], 0
	ds_read_b128 v[144:147], v168 offset:6144
	s_waitcnt lgkmcnt(6)
	v_mfma_f32_16x16x32_bf16 v[208:211], v[8:11], v[152:155], v[208:211]
	v_mfma_f32_16x16x32_bf16 v[212:215], v[12:15], v[152:155], v[212:215]
	ds_read_b128 v[148:151], v168 offset:6400
	ds_read_b128 v[24:27], v124 offset:6144
	ds_read_b128 v[28:31], v124 offset:6400
	s_waitcnt lgkmcnt(8)
	v_mfma_f32_16x16x32_bf16 v[216:219], v[8:11], v[156:159], v[216:219]
	v_mfma_f32_16x16x32_bf16 v[220:223], v[12:15], v[156:159], v[220:223]
	s_waitcnt lgkmcnt(4)
	v_mfma_f32_16x16x32_bf16 v[208:211], v[16:19], v[224:227], v[208:211]
	v_mfma_f32_16x16x32_bf16 v[212:215], v[20:23], v[224:227], v[212:215]
	v_mfma_f32_16x16x32_bf16 v[216:219], v[16:19], v[228:231], v[216:219]
	v_mfma_f32_16x16x32_bf16 v[220:223], v[20:23], v[228:231], v[220:223]
	s_waitcnt lgkmcnt(0)
	v_mfma_f32_16x16x32_bf16 v[208:211], v[24:27], v[144:147], v[208:211]
	v_mfma_f32_16x16x32_bf16 v[212:215], v[28:31], v[144:147], v[212:215]
	v_mfma_f32_16x16x32_bf16 v[216:219], v[24:27], v[148:151], v[216:219]
	v_mfma_f32_16x16x32_bf16 v[220:223], v[28:31], v[148:151], v[220:223]
	s_waitcnt vmcnt(8)
	s_barrier
	ds_read_b128 v[152:155], v168 offset:8192
	ds_read_b128 v[156:159], v168 offset:8448
	ds_read_b128 v[224:227], v168 offset:10240
	ds_read_b128 v[228:231], v168 offset:10496
	ds_read_b128 v[144:147], v168 offset:12288
	ds_read_b128 v[32:35], v124 offset:8192
	ds_read_b128 v[36:39], v124 offset:8448
	ds_read_b128 v[40:43], v124 offset:10240
	ds_read_b128 v[44:47], v124 offset:10496
	s_waitcnt lgkmcnt(2)
	v_mfma_f32_16x16x32_bf16 v[208:211], v[32:35], v[152:155], v[208:211]
	v_mfma_f32_16x16x32_bf16 v[212:215], v[36:39], v[152:155], v[212:215]
	ds_read_b128 v[148:151], v168 offset:12544
	ds_read_b128 v[48:51], v124 offset:12288
	ds_read_b128 v[52:55], v124 offset:12544
	v_mfma_f32_16x16x32_bf16 v[216:219], v[32:35], v[156:159], v[216:219]
	v_mfma_f32_16x16x32_bf16 v[220:223], v[36:39], v[156:159], v[220:223]
	ds_read_b128 v[152:155], v168 offset:14336
	s_waitcnt lgkmcnt(4)
	v_mfma_f32_16x16x32_bf16 v[208:211], v[40:43], v[224:227], v[208:211]
	v_mfma_f32_16x16x32_bf16 v[212:215], v[44:47], v[224:227], v[212:215]
	ds_read_b128 v[156:159], v168 offset:14592
	ds_read_b128 v[56:59], v124 offset:14336
	ds_read_b128 v[60:63], v124 offset:14592
	v_mfma_f32_16x16x32_bf16 v[216:219], v[40:43], v[228:231], v[216:219]
	v_mfma_f32_16x16x32_bf16 v[220:223], v[44:47], v[228:231], v[220:223]
	s_waitcnt lgkmcnt(4)
	v_mfma_f32_16x16x32_bf16 v[208:211], v[48:51], v[144:147], v[208:211]
	v_mfma_f32_16x16x32_bf16 v[212:215], v[52:55], v[144:147], v[212:215]
	v_mfma_f32_16x16x32_bf16 v[216:219], v[48:51], v[148:151], v[216:219]
	v_mfma_f32_16x16x32_bf16 v[220:223], v[52:55], v[148:151], v[220:223]
	s_waitcnt lgkmcnt(0)
	v_mfma_f32_16x16x32_bf16 v[208:211], v[56:59], v[152:155], v[208:211]
	v_mfma_f32_16x16x32_bf16 v[212:215], v[60:63], v[152:155], v[212:215]
	v_mfma_f32_16x16x32_bf16 v[216:219], v[56:59], v[156:159], v[216:219]
	v_mfma_f32_16x16x32_bf16 v[220:223], v[60:63], v[156:159], v[220:223]
	s_barrier
	s_add_i32 s60, s45, 4
	s_and_b32 s60, s60, 28
	s_lshl_b32 s60, s60, 15
	ds_read_b128 v[144:147], v169
	ds_read_b128 v[148:151], v169 offset:256
	ds_read_b128 v[152:155], v169 offset:2048
	ds_read_b128 v[156:159], v169 offset:2304
	ds_read_b128 v[224:227], v169 offset:4096
	s_waitcnt lgkmcnt(4)
	v_mfma_f32_16x16x32_bf16 v[136:139], v[0:3], v[144:147], 0
	v_mfma_f32_16x16x32_bf16 v[128:131], v[4:7], v[144:147], 0
	ds_read_b128 v[228:231], v169 offset:4352
	s_waitcnt lgkmcnt(4)
	v_mfma_f32_16x16x32_bf16 v[140:143], v[0:3], v[148:151], 0
	v_mfma_f32_16x16x32_bf16 v[132:135], v[4:7], v[148:151], 0
	ds_read_b128 v[144:147], v169 offset:6144
	s_waitcnt lgkmcnt(4)
	v_mfma_f32_16x16x32_bf16 v[136:139], v[8:11], v[152:155], v[136:139]
	v_mfma_f32_16x16x32_bf16 v[128:131], v[12:15], v[152:155], v[128:131]
	ds_read_b128 v[148:151], v169 offset:6400
	s_waitcnt lgkmcnt(4)
	v_mfma_f32_16x16x32_bf16 v[140:143], v[8:11], v[156:159], v[140:143]
	v_mfma_f32_16x16x32_bf16 v[132:135], v[12:15], v[156:159], v[132:135]
	ds_read_b128 v[152:155], v169 offset:8192
	s_waitcnt lgkmcnt(4)
	v_mfma_f32_16x16x32_bf16 v[136:139], v[16:19], v[224:227], v[136:139]
	v_mfma_f32_16x16x32_bf16 v[128:131], v[20:23], v[224:227], v[128:131]
	ds_read_b128 v[156:159], v169 offset:8448
	s_waitcnt lgkmcnt(4)
	v_mfma_f32_16x16x32_bf16 v[140:143], v[16:19], v[228:231], v[140:143]
	v_mfma_f32_16x16x32_bf16 v[132:135], v[20:23], v[228:231], v[132:135]
	ds_read_b128 v[224:227], v169 offset:10240
	s_waitcnt lgkmcnt(4)
	v_mfma_f32_16x16x32_bf16 v[136:139], v[24:27], v[144:147], v[136:139]
	v_mfma_f32_16x16x32_bf16 v[128:131], v[28:31], v[144:147], v[128:131]
	ds_read_b128 v[228:231], v169 offset:10496
	s_waitcnt lgkmcnt(4)
	v_mfma_f32_16x16x32_bf16 v[140:143], v[24:27], v[148:151], v[140:143]
	v_mfma_f32_16x16x32_bf16 v[132:135], v[28:31], v[148:151], v[132:135]
	ds_read_b128 v[144:147], v169 offset:12288
	s_waitcnt vmcnt(4)
	s_barrier
	s_waitcnt lgkmcnt(4)
	v_mfma_f32_16x16x32_bf16 v[136:139], v[32:35], v[152:155], v[136:139]
	v_mfma_f32_16x16x32_bf16 v[128:131], v[36:39], v[152:155], v[128:131]
	ds_read_b128 v[148:151], v169 offset:12544
	ds_read_b128 v[64:67], v124 offset:32768
	ds_read_b128 v[68:71], v124 offset:33024
	s_waitcnt lgkmcnt(6)
	v_mfma_f32_16x16x32_bf16 v[140:143], v[32:35], v[156:159], v[140:143]
	s_mov_b32 s61, s60
	s_mov_b32 m0, s25
	s_nop 0
	buffer_load_dwordx4 v166, s[12:15], s61 offen lds
	v_mfma_f32_16x16x32_bf16 v[132:135], v[36:39], v[156:159], v[132:135]
	ds_read_b128 v[152:155], v169 offset:14336
	s_waitcnt lgkmcnt(6)
	v_mfma_f32_16x16x32_bf16 v[136:139], v[40:43], v[224:227], v[136:139]
	v_mfma_f32_16x16x32_bf16 v[128:131], v[44:47], v[224:227], v[128:131]
	ds_read_b128 v[156:159], v169 offset:14592
	ds_read_b128 v[72:75], v124 offset:34816
	ds_read_b128 v[76:79], v124 offset:35072
	s_waitcnt lgkmcnt(8)
	v_mfma_f32_16x16x32_bf16 v[140:143], v[40:43], v[228:231], v[140:143]
	s_or_b32 s61, s60, 0x2000
	s_mov_b32 m0, s26
	s_nop 0
	buffer_load_dwordx4 v166, s[12:15], s61 offen lds
	v_mfma_f32_16x16x32_bf16 v[132:135], v[44:47], v[228:231], v[132:135]
	s_waitcnt lgkmcnt(7)
	v_mfma_f32_16x16x32_bf16 v[136:139], v[48:51], v[144:147], v[136:139]
	v_mfma_f32_16x16x32_bf16 v[128:131], v[52:55], v[144:147], v[128:131]
	ds_read_b128 v[80:83], v124 offset:36864
	ds_read_b128 v[84:87], v124 offset:37120
	s_waitcnt lgkmcnt(8)
	v_mfma_f32_16x16x32_bf16 v[140:143], v[48:51], v[148:151], v[140:143]
	s_or_b32 s61, s60, 0x8000
	s_mov_b32 m0, s27
	s_nop 0
	buffer_load_dwordx4 v166, s[12:15], s61 offen lds
	v_mfma_f32_16x16x32_bf16 v[132:135], v[52:55], v[148:151], v[132:135]
	s_waitcnt lgkmcnt(5)
	v_mfma_f32_16x16x32_bf16 v[136:139], v[56:59], v[152:155], v[136:139]
	v_mfma_f32_16x16x32_bf16 v[128:131], v[60:63], v[152:155], v[128:131]
	ds_read_b128 v[88:91], v124 offset:38912
	ds_read_b128 v[92:95], v124 offset:39168
	s_waitcnt lgkmcnt(6)
	v_mfma_f32_16x16x32_bf16 v[140:143], v[56:59], v[156:159], v[140:143]
	s_or_b32 s61, s60, 0xa000
	s_mov_b32 m0, s28
	s_nop 0
	buffer_load_dwordx4 v166, s[12:15], s61 offen lds
	v_mfma_f32_16x16x32_bf16 v[132:135], v[60:63], v[156:159], v[132:135]
	s_barrier
	s_add_i32 s60, s45, 4
	s_and_b32 s60, s60, 28
	s_or_b32 s60, s60, 2
	s_lshl_b32 s60, s60, 15
	ds_read_b128 v[144:147], v168 offset:32768
	ds_read_b128 v[148:151], v168 offset:33024
	ds_read_b128 v[152:155], v168 offset:34816
	ds_read_b128 v[156:159], v168 offset:35072
	ds_read_b128 v[224:227], v168 offset:36864
	s_waitcnt lgkmcnt(4)
	v_mfma_f32_16x16x32_bf16 v[208:211], v[64:67], v[144:147], v[208:211]
	v_mfma_f32_16x16x32_bf16 v[212:215], v[68:71], v[144:147], v[212:215]
	ds_read_b128 v[228:231], v168 offset:37120
	s_waitcnt lgkmcnt(4)
	v_mfma_f32_16x16x32_bf16 v[216:219], v[64:67], v[148:151], v[216:219]
	s_mov_b32 s61, s60
	s_mov_b32 m0, s34
	s_nop 0
	buffer_load_dwordx4 v166, s[12:15], s61 offen lds
	v_mfma_f32_16x16x32_bf16 v[220:223], v[68:71], v[148:151], v[220:223]
	ds_read_b128 v[144:147], v168 offset:38912
	s_waitcnt lgkmcnt(4)
	v_mfma_f32_16x16x32_bf16 v[208:211], v[72:75], v[152:155], v[208:211]
	v_mfma_f32_16x16x32_bf16 v[212:215], v[76:79], v[152:155], v[212:215]
	ds_read_b128 v[148:151], v168 offset:39168
	s_waitcnt lgkmcnt(4)
	v_mfma_f32_16x16x32_bf16 v[216:219], v[72:75], v[156:159], v[216:219]
	v_mfma_f32_16x16x32_bf16 v[220:223], v[76:79], v[156:159], v[220:223]
	s_waitcnt lgkmcnt(3)
	v_mfma_f32_16x16x32_bf16 v[208:211], v[80:83], v[224:227], v[208:211]
	v_mfma_f32_16x16x32_bf16 v[212:215], v[84:87], v[224:227], v[212:215]
	s_waitcnt lgkmcnt(2)
	v_mfma_f32_16x16x32_bf16 v[216:219], v[80:83], v[228:231], v[216:219]
	s_or_b32 s61, s60, 0x2000
	s_mov_b32 m0, s35
	s_nop 0
	buffer_load_dwordx4 v166, s[12:15], s61 offen lds
	v_mfma_f32_16x16x32_bf16 v[220:223], v[84:87], v[228:231], v[220:223]
	s_waitcnt lgkmcnt(1)
	v_mfma_f32_16x16x32_bf16 v[208:211], v[88:91], v[144:147], v[208:211]
	v_mfma_f32_16x16x32_bf16 v[212:215], v[92:95], v[144:147], v[212:215]
	s_waitcnt lgkmcnt(0)
	v_mfma_f32_16x16x32_bf16 v[216:219], v[88:91], v[148:151], v[216:219]
	v_mfma_f32_16x16x32_bf16 v[220:223], v[92:95], v[148:151], v[220:223]
	s_waitcnt vmcnt(6)
	s_barrier
	ds_read_b128 v[152:155], v168 offset:40960
	ds_read_b128 v[156:159], v168 offset:41216
	ds_read_b128 v[224:227], v168 offset:43008
	ds_read_b128 v[228:231], v168 offset:43264
	ds_read_b128 v[144:147], v168 offset:45056
	ds_read_b128 v[96:99], v124 offset:40960
	ds_read_b128 v[100:103], v124 offset:41216
	ds_read_b128 v[104:107], v124 offset:43008
	ds_read_b128 v[108:111], v124 offset:43264
	s_waitcnt lgkmcnt(2)
	v_mfma_f32_16x16x32_bf16 v[208:211], v[96:99], v[152:155], v[208:211]
	v_mfma_f32_16x16x32_bf16 v[212:215], v[100:103], v[152:155], v[212:215]
	ds_read_b128 v[148:151], v168 offset:45312
	ds_read_b128 v[112:115], v124 offset:45056
	ds_read_b128 v[116:119], v124 offset:45312
	v_mfma_f32_16x16x32_bf16 v[216:219], v[96:99], v[156:159], v[216:219]
	s_or_b32 s61, s60, 0x8000
	s_mov_b32 m0, s36
	s_nop 0
	buffer_load_dwordx4 v166, s[12:15], s61 offen lds
	v_mfma_f32_16x16x32_bf16 v[220:223], v[100:103], v[156:159], v[220:223]
	ds_read_b128 v[152:155], v168 offset:47104
	s_waitcnt lgkmcnt(4)
	v_mfma_f32_16x16x32_bf16 v[208:211], v[104:107], v[224:227], v[208:211]
	v_mfma_f32_16x16x32_bf16 v[212:215], v[108:111], v[224:227], v[212:215]
	ds_read_b128 v[156:159], v168 offset:47360
	ds_read_b128 v[120:123], v124 offset:47104
	ds_read_b128 v[124:127], v124 offset:47360
	v_mfma_f32_16x16x32_bf16 v[216:219], v[104:107], v[228:231], v[216:219]
	v_mfma_f32_16x16x32_bf16 v[220:223], v[108:111], v[228:231], v[220:223]
	s_waitcnt lgkmcnt(4)
	v_mfma_f32_16x16x32_bf16 v[208:211], v[112:115], v[144:147], v[208:211]
	v_mfma_f32_16x16x32_bf16 v[212:215], v[116:119], v[144:147], v[212:215]
	v_mfma_f32_16x16x32_bf16 v[216:219], v[112:115], v[148:151], v[216:219]
	s_or_b32 s61, s60, 0xa000
	s_mov_b32 m0, s37
	s_nop 0
	buffer_load_dwordx4 v166, s[12:15], s61 offen lds
	v_mfma_f32_16x16x32_bf16 v[220:223], v[116:119], v[148:151], v[220:223]
	s_waitcnt lgkmcnt(0)
	v_mfma_f32_16x16x32_bf16 v[208:211], v[120:123], v[152:155], v[208:211]
	v_mfma_f32_16x16x32_bf16 v[212:215], v[124:127], v[152:155], v[212:215]
	v_mfma_f32_16x16x32_bf16 v[216:219], v[120:123], v[156:159], v[216:219]
	v_mfma_f32_16x16x32_bf16 v[220:223], v[124:127], v[156:159], v[220:223]
	s_waitcnt vmcnt(4)
	s_barrier
	s_nop 7
	s_nop 3
	s_cmp_lg_u32 s8, s43
	s_cbranch_scc1 .Ldiag0_done
	s_mov_b64 s[56:57], exec
	s_and_b64 exec, s[56:57], s[0:1]
	global_store_dword v[164:165], v208, off
	v_mov_b32_e32 v208, -1.0
	global_store_dword v[164:165], v220, off offset:64
	v_mov_b32_e32 v220, -1.0
	s_and_b64 exec, s[56:57], s[2:3]
	global_store_dword v[164:165], v209, off
	v_mov_b32_e32 v209, -1.0
	global_store_dword v[164:165], v221, off offset:64
	v_mov_b32_e32 v221, -1.0
	s_and_b64 exec, s[56:57], s[4:5]
	global_store_dword v[164:165], v210, off
	v_mov_b32_e32 v210, -1.0
	global_store_dword v[164:165], v222, off offset:64
	v_mov_b32_e32 v222, -1.0
	s_and_b64 exec, s[56:57], s[6:7]
	global_store_dword v[164:165], v211, off
	v_mov_b32_e32 v211, -1.0
	global_store_dword v[164:165], v223, off offset:64
	v_mov_b32_e32 v223, -1.0
	s_mov_b64 exec, s[56:57]
